# baseline (speedup 1.0000x reference)
.LBB2_12:
	s_or_b64 exec, exec, s[12:13]
	v_lshlrev_b32_e32 v106, 9, v119
	v_ffbl_b32_e32 v107, v107
	v_ffbl_b32_e32 v108, v108
	v_lshlrev_b32_e32 v116, 25, v119
	v_lshl_or_b32 v107, v107, 4, v106
	v_mov_b32_e32 v109, 0x2000
	v_lshl_or_b32 v108, v108, 20, v116
	v_bfrev_b32_e32 v116, 4
	v_ffbl_b32_e32 v0, v0
	v_cndmask_b32_e64 v107, v107, v109, s[8:9]
	v_cndmask_b32_e64 v108, v108, v116, s[4:5]
	v_lshl_or_b32 v0, v0, 4, v106
	v_cndmask_b32_e32 v0, v0, v109, vcc
	v_or_b32_e32 v106, v108, v107
	v_mov_b32_e32 v108, 0x800000
	v_lshlrev_b32_e32 v107, 16, v117
	v_cndmask_b32_e64 v108, 0, v108, s[6:7]
	s_waitcnt lgkmcnt(2)
	v_lshl_or_b32 v0, v118, 24, v0
	v_or3_b32 v0, v0, v108, v107
	ds_write2_b32 v105, v106, v0 offset0:1 offset1:3
	v_cmp_ne_u32_e32 vcc, 0, v140
	v_cmp_ne_u32_e64 s[22:23], 0, v141
	v_lshlrev_b32_e32 v150, 5, v113
	v_lshl_add_u32 v155, v113, 2, v115
	v_lshlrev_b32_e32 v155, 2, v155
	v_add_u32_e32 v155, 0x11840, v155
	v_lshrrev_b64 v[146:147], v150, vcc
	v_lshrrev_b64 v[156:157], v150, s[22:23]
	v_mov_b32_e32 v151, 0x400
	v_cmp_ne_u32_e32 vcc, 0, v146
	v_cmp_ne_u32_e64 s[22:23], 0, v156
	s_nop 1
	v_cndmask_b32_e32 v146, 0, v151, vcc
	v_cndmask_b32_e64 v156, 0, v151, s[22:23]
	v_cmp_eq_u32_e32 vcc, 0, v111
	s_and_saveexec_b64 s[22:23], vcc
	ds_or_b32 v155, v146
	ds_or_b32 v155, v156 offset:32
	s_or_b64 exec, exec, s[22:23]
	s_movk_i32 s2, 0x2010
	v_mul_u32_u24_e32 v105, 0x2010, v115
	v_cmp_eq_u32_e32 vcc, 0, v114
	s_waitcnt vmcnt(22)
	ds_write_b128 v104, v[38:41] offset:32832
	s_waitcnt vmcnt(21)
	ds_write_b128 v104, v[42:45] offset:36928
	s_waitcnt vmcnt(20)
	ds_write_b128 v104, v[46:49] offset:41024
	s_waitcnt vmcnt(19)
	ds_write_b128 v104, v[50:53] offset:45120
	s_waitcnt vmcnt(18)
	ds_write_b128 v104, v[54:57] offset:49216
	s_waitcnt vmcnt(17)
	ds_write_b128 v104, v[66:69] offset:53312
	s_and_saveexec_b64 s[0:1], vcc
	v_mov_b32_e32 v38, 0
	v_mov_b32_e32 v39, v38
	v_mov_b32_e32 v40, v38
	v_mov_b32_e32 v41, v38
	ds_write_b128 v105, v[38:41] offset:8192
	s_or_b64 exec, exec, s[0:1]
	v_lshlrev_b32_e32 v40, 3, v113
	v_lshlrev_b32_e32 v67, 4, v110
	v_or_b32_e32 v38, 0x1e0, v111
	v_or_b32_e32 v0, 0x8040, v40
	v_mad_u32_u24 v66, v1, s2, v67
	v_mad_u32_u24 v38, v38, 48, v0
	s_waitcnt vmcnt(16)
	ds_write_b128 v66, v[58:61]
	s_waitcnt vmcnt(15)
	ds_write_b128 v66, v[62:65] offset:1024
	s_waitcnt vmcnt(14)
	ds_write_b128 v66, v[70:73] offset:2048
	s_waitcnt vmcnt(13)
	ds_write_b128 v66, v[74:77] offset:3072
	s_waitcnt vmcnt(12)
	ds_write_b128 v66, v[78:81] offset:4096
	s_waitcnt vmcnt(11)
	ds_write_b128 v66, v[82:85] offset:5120
	s_waitcnt vmcnt(10)
	ds_write_b128 v66, v[86:89] offset:6144
	s_waitcnt vmcnt(9)
	ds_write_b128 v66, v[90:93] offset:7168
	s_waitcnt lgkmcnt(0)
	s_barrier
	v_lshl_add_u32 v116, v113, 3, v105
	v_or_b32_e32 v106, 0x1e0, v111
	v_lshlrev_b32_e32 v138, 4, v106
	v_lshlrev_b32_e32 v139, 3, v106
	v_add_u32_e32 v139, 0x118c0, v139
	v_mul_u32_u24_e32 v156, 48, v106
	v_add_u32_e32 v156, v0, v156
	v_mov_b32_e32 v157, 0x1187c
	v_add_u32_e32 v137, v116, v138
	v_add_u32_e32 v138, 0x200, v138
	v_lshlrev_b32_e32 v160, 4, v111
	v_lshlrev_b32_e32 v161, 3, v111
	v_add_u32_e32 v161, 0x118c0, v161
	v_mul_u32_u24_e32 v162, 48, v111
	v_add_u32_e32 v162, v0, v162
	v_mov_b32_e32 v163, 0x11840
	v_mul_hi_u32_u24_e32 v159, 0x410, v111
	v_mul_u32_u24_e32 v158, 0x410, v111
	v_mov_b32_e32 v107, 0x82000
	v_mad_u64_u32 v[158:159], s[0:1], s20, v107, v[158:159]
	v_lshlrev_b32_e32 v107, 3, v113
	v_or_b32_e32 v158, v158, v107
	v_lshl_add_u64 v[158:159], s[14:15], 0, v[158:159]
	s_mov_b64 s[0:1], 0x79e30
	s_mov_b32 s2, 0xffff7e00
	s_mov_b32 s3, -1
	v_lshl_add_u64 v[158:159], v[158:159], 0, s[0:1]
	ds_read_b128 v[38:41], v138 offset:56896
	ds_read_b64 v[42:43], v139
	ds_read2_b64 v[56:59], v156 offset1:2
	v_lshl_add_u32 v107, v114, 2, v163
	v_add_u32_e32 v107, -8, v107
	ds_read_b32 v60, v107
	v_add_u32_e32 v156, 0xfffffa00, v156
	ds_read2_b64 v[52:55], v156 offset1:2
	v_add_u32_e32 v106, -2, v114
	v_cmp_gt_u32_e32 vcc, 16, v106
	s_waitcnt lgkmcnt(0)
	v_cndmask_b32_e32 v60, 0, v60, vcc
	s_nop 1
	v_readlane_b32 s4, v60, 17
	v_readlane_b32 s21, v60, 16
	v_add_u32_sdwa v92, v105, v56 dst_sel:DWORD dst_unused:UNUSED_PAD src0_sel:DWORD src1_sel:WORD_0
	v_add_u32_sdwa v93, v105, v56 dst_sel:DWORD dst_unused:UNUSED_PAD src0_sel:DWORD src1_sel:WORD_1
	v_add_u32_sdwa v106, v105, v57 dst_sel:DWORD dst_unused:UNUSED_PAD src0_sel:DWORD src1_sel:WORD_0
	v_add_u32_sdwa v107, v105, v57 dst_sel:DWORD dst_unused:UNUSED_PAD src0_sel:DWORD src1_sel:WORD_1
	v_add_u32_sdwa v108, v105, v58 dst_sel:DWORD dst_unused:UNUSED_PAD src0_sel:DWORD src1_sel:WORD_0
	v_add_u32_sdwa v109, v105, v58 dst_sel:DWORD dst_unused:UNUSED_PAD src0_sel:DWORD src1_sel:WORD_1
	v_add_u32_sdwa v88, v105, v59 dst_sel:DWORD dst_unused:UNUSED_PAD src0_sel:DWORD src1_sel:WORD_0
	v_add_u32_sdwa v89, v105, v59 dst_sel:DWORD dst_unused:UNUSED_PAD src0_sel:DWORD src1_sel:WORD_1
	ds_read_b128 v[120:123], v92
	ds_read_b128 v[124:127], v93
	ds_read_b128 v[128:131], v106
	ds_read_b128 v[132:135], v107
	ds_read_b128 v[140:143], v108
	ds_read_b128 v[144:147], v109
	ds_read_b128 v[148:151], v88
	ds_read_b128 v[152:155], v89
	s_waitcnt lgkmcnt(0)
	v_pk_add_f32 v[120:121], v[120:121], v[124:125]
	v_pk_add_f32 v[122:123], v[122:123], v[126:127]
	v_pk_add_f32 v[128:129], v[128:129], v[132:133]
	v_pk_add_f32 v[130:131], v[130:131], v[134:135]
	v_pk_add_f32 v[140:141], v[140:141], v[144:145]
	v_pk_add_f32 v[142:143], v[142:143], v[146:147]
	v_pk_add_f32 v[148:149], v[148:149], v[152:153]
	v_pk_add_f32 v[150:151], v[150:151], v[154:155]
	s_bitcmp1_b32 s4, 8
	s_cbranch_scc1 .Lfarslow_pre
.Lfarslow_ret_pre:
	v_pk_add_f32 v[120:121], v[120:121], v[128:129]
	v_pk_add_f32 v[122:123], v[122:123], v[130:131]
	v_pk_add_f32 v[140:141], v[140:141], v[148:149]
	v_pk_add_f32 v[142:143], v[142:143], v[150:151]
	v_pk_add_f32 v[120:121], v[120:121], v[140:141]
	v_pk_add_f32 v[122:123], v[122:123], v[142:143]
	s_nop 1
	v_permlane32_swap_b32_e32 v120, v122
	v_permlane32_swap_b32_e32 v121, v123
	v_pk_add_f32 v[44:45], v[120:121], v[122:123]
	v_add_u32_e32 v138, 0xfffffe00, v138
	v_add_u32_e32 v139, 0xffffff00, v139
	v_add_u32_e32 v156, 0xfffffa00, v156
	v_lshl_add_u64 v[158:159], v[158:159], 0, s[2:3]
	s_mov_b32 s5, 15

.Lit_Af:
	v_add_u32_sdwa v88, v116, v42 dst_sel:DWORD dst_unused:UNUSED_PAD src0_sel:DWORD src1_sel:WORD_0
	v_add_u32_sdwa v89, v116, v42 dst_sel:DWORD dst_unused:UNUSED_PAD src0_sel:DWORD src1_sel:WORD_1
	ds_read_b64 v[68:69], v88
	v_add_u32_sdwa v90, v116, v43 dst_sel:DWORD dst_unused:UNUSED_PAD src0_sel:DWORD src1_sel:WORD_0
	ds_read_b64 v[70:71], v89
	v_add_u32_sdwa v91, v116, v43 dst_sel:DWORD dst_unused:UNUSED_PAD src0_sel:DWORD src1_sel:WORD_1
	ds_read_b64 v[72:73], v90
	ds_read_b64 v[74:75], v91
	v_add_u32_sdwa v92, v105, v52 dst_sel:DWORD dst_unused:UNUSED_PAD src0_sel:DWORD src1_sel:WORD_0
	v_add_u32_sdwa v93, v105, v52 dst_sel:DWORD dst_unused:UNUSED_PAD src0_sel:DWORD src1_sel:WORD_1
	v_add_u32_sdwa v106, v105, v53 dst_sel:DWORD dst_unused:UNUSED_PAD src0_sel:DWORD src1_sel:WORD_0
	v_add_u32_sdwa v107, v105, v53 dst_sel:DWORD dst_unused:UNUSED_PAD src0_sel:DWORD src1_sel:WORD_1
	v_add_u32_sdwa v108, v105, v54 dst_sel:DWORD dst_unused:UNUSED_PAD src0_sel:DWORD src1_sel:WORD_0
	v_add_u32_sdwa v109, v105, v54 dst_sel:DWORD dst_unused:UNUSED_PAD src0_sel:DWORD src1_sel:WORD_1
	v_add_u32_sdwa v88, v105, v55 dst_sel:DWORD dst_unused:UNUSED_PAD src0_sel:DWORD src1_sel:WORD_0
	v_add_u32_sdwa v89, v105, v55 dst_sel:DWORD dst_unused:UNUSED_PAD src0_sel:DWORD src1_sel:WORD_1
	ds_read_b128 v[120:123], v92
	ds_read_b128 v[124:127], v93
	ds_read_b128 v[128:131], v106
	ds_read_b128 v[132:135], v107
	ds_read_b128 v[140:143], v108
	ds_read_b128 v[144:147], v109
	ds_read_b128 v[148:151], v88
	ds_read_b128 v[152:155], v89
	v_add_u32_sdwa v118, v116, v39 dst_sel:DWORD dst_unused:UNUSED_PAD src0_sel:DWORD src1_sel:WORD_0
	s_waitcnt lgkmcnt(11)
	v_pk_add_f32 v[76:77], v[44:45], v[68:69]
	s_waitcnt lgkmcnt(9)
	v_pk_add_f32 v[78:79], v[70:71], v[72:73]
	s_waitcnt lgkmcnt(8)
	v_pk_add_f32 v[76:77], v[76:77], v[74:75]
	v_bfe_u32 v117, v41, 16, 7
	v_pk_add_f32 v[76:77], v[76:77], v[78:79]
	v_add_u32_sdwa v119, v116, v39 dst_sel:DWORD dst_unused:UNUSED_PAD src0_sel:DWORD src1_sel:WORD_1
	v_pk_mul_f32 v[78:79], v[40:41], v[76:77] op_sel_hi:[0,1]
	v_add_u32_sdwa v136, v116, v41 dst_sel:DWORD dst_unused:UNUSED_PAD src0_sel:DWORD src1_sel:WORD_0
	ds_write_b64 v137, v[78:79]
	ds_read_b128 v[46:49], v138 offset:56896
	ds_read_b64 v[50:51], v139
	ds_read2_b64 v[56:59], v156 offset1:2
	v_cmp_eq_u32_e64 s[6:7], 1, v117
	s_waitcnt lgkmcnt(3)
	ds_read_b64 v[82:83], v118
	ds_read_b64 v[84:85], v119
	ds_read_b64 v[86:87], v136
	v_pk_add_f32 v[120:121], v[120:121], v[124:125]
	v_pk_add_f32 v[122:123], v[122:123], v[126:127]
	v_pk_add_f32 v[128:129], v[128:129], v[132:133]
	v_pk_add_f32 v[130:131], v[130:131], v[134:135]
	v_pk_add_f32 v[140:141], v[140:141], v[144:145]
	v_pk_add_f32 v[142:143], v[142:143], v[146:147]
	v_pk_add_f32 v[148:149], v[148:149], v[152:153]
	v_pk_add_f32 v[150:151], v[150:151], v[154:155]
	v_pk_add_f32 v[120:121], v[120:121], v[128:129]
	v_pk_add_f32 v[122:123], v[122:123], v[130:131]
	v_pk_add_f32 v[140:141], v[140:141], v[148:149]
	v_pk_add_f32 v[142:143], v[142:143], v[150:151]
	v_pk_add_f32 v[120:121], v[120:121], v[140:141]
	v_pk_add_f32 v[122:123], v[122:123], v[142:143]
	v_add_u32_e32 v138, 0xfffffe00, v138
	v_add_u32_e32 v139, 0xffffff00, v139
	v_permlane32_swap_b32_e32 v120, v122
	v_permlane32_swap_b32_e32 v121, v123
	v_pk_add_f32 v[62:63], v[120:121], v[122:123]
	s_mov_b64 exec, s[6:7]
	s_waitcnt lgkmcnt(2)
	v_pk_fma_f32 v[80:81], v[40:41], v[82:83], v[78:79] op_sel_hi:[0,1,1]
	s_waitcnt lgkmcnt(1)
	v_pk_fma_f32 v[80:81], v[40:41], v[84:85], v[80:81] op_sel_hi:[0,1,1]
	s_waitcnt lgkmcnt(0)
	v_pk_fma_f32 v[80:81], v[40:41], v[86:87], v[80:81] op_sel_hi:[0,1,1]
	ds_write_b64 v137, v[80:81]
	s_mov_b64 exec, -1
	s_cmp_lt_u32 s9, 2
	s_cbranch_scc1 .Lend_A
	s_mov_b32 s8, 2

.Lend_A:
	s_waitcnt lgkmcnt(0)
	v_add_u32_e32 v156, 0xfffffa00, v156
	v_add_u32_e32 v137, 0xfffffe00, v137
	v_max_i32_e32 v156, v156, v162
	v_lshl_add_u64 v[158:159], v[158:159], 0, s[2:3]
	v_readlane_b32 s4, v60, s5
	s_sub_u32 s5, s5, 1
	s_or_b32 s10, s21, s4
	s_and_b32 s10, s10, 0x700
	s_cbranch_scc1 .Lit_Bs
	s_and_b32 s9, s21, 0xff
	s_cbranch_scc0 .Lit_Bs
.Lit_Bf:
	v_add_u32_sdwa v88, v116, v50 dst_sel:DWORD dst_unused:UNUSED_PAD src0_sel:DWORD src1_sel:WORD_0
	v_add_u32_sdwa v89, v116, v50 dst_sel:DWORD dst_unused:UNUSED_PAD src0_sel:DWORD src1_sel:WORD_1
	ds_read_b64 v[68:69], v88
	v_add_u32_sdwa v90, v116, v51 dst_sel:DWORD dst_unused:UNUSED_PAD src0_sel:DWORD src1_sel:WORD_0
	ds_read_b64 v[70:71], v89
	v_add_u32_sdwa v91, v116, v51 dst_sel:DWORD dst_unused:UNUSED_PAD src0_sel:DWORD src1_sel:WORD_1
	ds_read_b64 v[72:73], v90
	ds_read_b64 v[74:75], v91
	v_add_u32_sdwa v92, v105, v56 dst_sel:DWORD dst_unused:UNUSED_PAD src0_sel:DWORD src1_sel:WORD_0
	v_add_u32_sdwa v93, v105, v56 dst_sel:DWORD dst_unused:UNUSED_PAD src0_sel:DWORD src1_sel:WORD_1
	v_add_u32_sdwa v106, v105, v57 dst_sel:DWORD dst_unused:UNUSED_PAD src0_sel:DWORD src1_sel:WORD_0
	v_add_u32_sdwa v107, v105, v57 dst_sel:DWORD dst_unused:UNUSED_PAD src0_sel:DWORD src1_sel:WORD_1
	v_add_u32_sdwa v108, v105, v58 dst_sel:DWORD dst_unused:UNUSED_PAD src0_sel:DWORD src1_sel:WORD_0
	v_add_u32_sdwa v109, v105, v58 dst_sel:DWORD dst_unused:UNUSED_PAD src0_sel:DWORD src1_sel:WORD_1
	v_add_u32_sdwa v88, v105, v59 dst_sel:DWORD dst_unused:UNUSED_PAD src0_sel:DWORD src1_sel:WORD_0
	v_add_u32_sdwa v89, v105, v59 dst_sel:DWORD dst_unused:UNUSED_PAD src0_sel:DWORD src1_sel:WORD_1
	ds_read_b128 v[120:123], v92
	ds_read_b128 v[124:127], v93
	ds_read_b128 v[128:131], v106
	ds_read_b128 v[132:135], v107
	ds_read_b128 v[140:143], v108
	ds_read_b128 v[144:147], v109
	ds_read_b128 v[148:151], v88
	ds_read_b128 v[152:155], v89
	v_add_u32_sdwa v118, v116, v47 dst_sel:DWORD dst_unused:UNUSED_PAD src0_sel:DWORD src1_sel:WORD_0
	s_waitcnt lgkmcnt(11)
	v_pk_add_f32 v[76:77], v[62:63], v[68:69]
	s_waitcnt lgkmcnt(9)
	v_pk_add_f32 v[78:79], v[70:71], v[72:73]
	s_waitcnt lgkmcnt(8)
	v_pk_add_f32 v[76:77], v[76:77], v[74:75]
	v_bfe_u32 v117, v49, 16, 7
	v_pk_add_f32 v[76:77], v[76:77], v[78:79]
	v_add_u32_sdwa v119, v116, v47 dst_sel:DWORD dst_unused:UNUSED_PAD src0_sel:DWORD src1_sel:WORD_1
	v_pk_mul_f32 v[78:79], v[48:49], v[76:77] op_sel_hi:[0,1]
	v_add_u32_sdwa v136, v116, v49 dst_sel:DWORD dst_unused:UNUSED_PAD src0_sel:DWORD src1_sel:WORD_0
	ds_write_b64 v137, v[78:79]
	ds_read_b128 v[38:41], v138 offset:56896
	ds_read_b64 v[42:43], v139
	ds_read2_b64 v[52:55], v156 offset1:2
	v_cmp_eq_u32_e64 s[6:7], 1, v117
	s_waitcnt lgkmcnt(3)
	ds_read_b64 v[82:83], v118
	ds_read_b64 v[84:85], v119
	ds_read_b64 v[86:87], v136
	v_pk_add_f32 v[120:121], v[120:121], v[124:125]
	v_pk_add_f32 v[122:123], v[122:123], v[126:127]
	v_pk_add_f32 v[128:129], v[128:129], v[132:133]
	v_pk_add_f32 v[130:131], v[130:131], v[134:135]
	v_pk_add_f32 v[140:141], v[140:141], v[144:145]
	v_pk_add_f32 v[142:143], v[142:143], v[146:147]
	v_pk_add_f32 v[148:149], v[148:149], v[152:153]
	v_pk_add_f32 v[150:151], v[150:151], v[154:155]
	v_pk_add_f32 v[120:121], v[120:121], v[128:129]
	v_pk_add_f32 v[122:123], v[122:123], v[130:131]
	v_pk_add_f32 v[140:141], v[140:141], v[148:149]
	v_pk_add_f32 v[142:143], v[142:143], v[150:151]
	v_pk_add_f32 v[120:121], v[120:121], v[140:141]
	v_pk_add_f32 v[122:123], v[122:123], v[142:143]
	v_add_u32_e32 v138, 0xfffffe00, v138
	v_add_u32_e32 v139, 0xffffff00, v139
	v_permlane32_swap_b32_e32 v120, v122
	v_permlane32_swap_b32_e32 v121, v123
	v_pk_add_f32 v[44:45], v[120:121], v[122:123]
	s_mov_b64 exec, s[6:7]
	s_waitcnt lgkmcnt(2)
	v_pk_fma_f32 v[80:81], v[48:49], v[82:83], v[78:79] op_sel_hi:[0,1,1]
	s_waitcnt lgkmcnt(1)
	v_pk_fma_f32 v[80:81], v[48:49], v[84:85], v[80:81] op_sel_hi:[0,1,1]
	s_waitcnt lgkmcnt(0)
	v_pk_fma_f32 v[80:81], v[48:49], v[86:87], v[80:81] op_sel_hi:[0,1,1]
	ds_write_b64 v137, v[80:81]
	s_mov_b64 exec, -1
	s_cmp_lt_u32 s9, 2
	s_cbranch_scc1 .Lend_B
	s_mov_b32 s8, 2

.Lend_B:
	s_waitcnt lgkmcnt(0)
	v_add_u32_e32 v156, 0xfffffa00, v156
	v_add_u32_e32 v137, 0xfffffe00, v137
	v_max_i32_e32 v156, v156, v162
	v_lshl_add_u64 v[158:159], v[158:159], 0, s[2:3]
	v_readlane_b32 s21, v60, s5
	s_cmp_eq_u32 s5, 0
	s_cbranch_scc1 .Lchain_done
	s_sub_u32 s5, s5, 1
	s_branch .Lchain_top

.Lnearslow_ret_As:
	v_pk_mul_f32 v[78:79], v[40:41], v[76:77] op_sel_hi:[0,1]
	v_add_u32_sdwa v136, v116, v41 dst_sel:DWORD dst_unused:UNUSED_PAD src0_sel:DWORD src1_sel:WORD_0
	ds_write_b64 v137, v[78:79]
	ds_read_b128 v[46:49], v138 offset:56896
	ds_read_b64 v[50:51], v139
	ds_read2_b64 v[56:59], v156 offset1:2
	s_and_b32 s9, s4, 0xff
	v_cmp_eq_u32_e64 s[6:7], 1, v117
	s_waitcnt lgkmcnt(3)
	s_bitcmp1_b32 s4, 9
	s_cbranch_scc1 .Lfs_As
	s_cmp_eq_u32 s9, 0
	s_cbranch_scc1 .Lfs_As
	ds_read_b64 v[82:83], v118
	ds_read_b64 v[84:85], v119
	ds_read_b64 v[86:87], v136

.Lnearslow_ret_Bs:
	v_pk_mul_f32 v[78:79], v[48:49], v[76:77] op_sel_hi:[0,1]
	v_add_u32_sdwa v136, v116, v49 dst_sel:DWORD dst_unused:UNUSED_PAD src0_sel:DWORD src1_sel:WORD_0
	ds_write_b64 v137, v[78:79]
	ds_read_b128 v[38:41], v138 offset:56896
	ds_read_b64 v[42:43], v139
	ds_read2_b64 v[52:55], v156 offset1:2
	s_and_b32 s9, s21, 0xff
	v_cmp_eq_u32_e64 s[6:7], 1, v117
	s_waitcnt lgkmcnt(3)
	s_bitcmp1_b32 s21, 9
	s_cbranch_scc1 .Lfs_Bs
	s_cmp_eq_u32 s9, 0
	s_cbranch_scc1 .Lfs_Bs
	ds_read_b64 v[82:83], v118
	ds_read_b64 v[84:85], v119
	ds_read_b64 v[86:87], v136
